# speedup vs baseline: 1.0008x; 1.0008x over previous
_Z15score_ds_kernelPKfS0_S0_S0_S0_S0_PfPKDF16_:
	s_load_dwordx2 s[26:27], s[0:1], 0x38
	s_bfe_u32 s28, s2, 0x10003
	s_mul_i32 s28, s28, 0x1a400
	v_lshlrev_b32_e32 v254, 4, v0
	v_mov_b32_e32 v255, 0
	v_readfirstlane_b32 s29, v0
	s_mov_b64 s[30:31], 0x2000
	s_waitcnt lgkmcnt(0)
	s_add_u32 s26, s26, s28
	s_addc_u32 s27, s27, 0
	s_lshl_b32 s28, s29, 4
	v_lshl_add_u64 v[254:255], s[26:27], 0, v[254:255]
	s_mov_b32 m0, s28
	s_add_u32 s28, s28, 0x2000
	global_load_lds_dwordx4 v[254:255], off
	v_lshl_add_u64 v[254:255], v[254:255], 0, s[30:31]
	s_mov_b32 m0, s28
	s_add_u32 s28, s28, 0x2000
	global_load_lds_dwordx4 v[254:255], off
	v_lshl_add_u64 v[254:255], v[254:255], 0, s[30:31]
	s_mov_b32 m0, s28
	s_add_u32 s28, s28, 0x2000
	global_load_lds_dwordx4 v[254:255], off
	v_lshl_add_u64 v[254:255], v[254:255], 0, s[30:31]
	s_mov_b32 m0, s28
	s_add_u32 s28, s28, 0x2000
	global_load_lds_dwordx4 v[254:255], off
	v_lshl_add_u64 v[254:255], v[254:255], 0, s[30:31]
	s_mov_b32 m0, s28
	s_add_u32 s28, s28, 0x2000
	global_load_lds_dwordx4 v[254:255], off
	v_lshl_add_u64 v[254:255], v[254:255], 0, s[30:31]
	s_mov_b32 m0, s28
	s_add_u32 s28, s28, 0x2000
	global_load_lds_dwordx4 v[254:255], off
	v_lshl_add_u64 v[254:255], v[254:255], 0, s[30:31]
	s_mov_b32 m0, s28
	s_add_u32 s28, s28, 0x2000
	global_load_lds_dwordx4 v[254:255], off
	v_lshl_add_u64 v[254:255], v[254:255], 0, s[30:31]
	s_mov_b32 m0, s28
	s_add_u32 s28, s28, 0x2000
	global_load_lds_dwordx4 v[254:255], off
	v_lshl_add_u64 v[254:255], v[254:255], 0, s[30:31]
	s_mov_b32 m0, s28
	s_add_u32 s28, s28, 0x2000
	global_load_lds_dwordx4 v[254:255], off
	v_lshl_add_u64 v[254:255], v[254:255], 0, s[30:31]
	s_mov_b32 m0, s28
	s_add_u32 s28, s28, 0x2000
	global_load_lds_dwordx4 v[254:255], off
	v_lshl_add_u64 v[254:255], v[254:255], 0, s[30:31]
	s_mov_b32 m0, s28
	s_add_u32 s28, s28, 0x2000
	global_load_lds_dwordx4 v[254:255], off
	v_lshl_add_u64 v[254:255], v[254:255], 0, s[30:31]
	s_mov_b32 m0, s28
	s_add_u32 s28, s28, 0x2000
	global_load_lds_dwordx4 v[254:255], off
	v_lshl_add_u64 v[254:255], v[254:255], 0, s[30:31]
	s_mov_b32 m0, s28
	s_add_u32 s28, s28, 0x2000
	global_load_lds_dwordx4 v[254:255], off
	v_lshl_add_u64 v[254:255], v[254:255], 0, s[30:31]
	s_cmp_lg_u32 s29, 0
	s_cbranch_scc1 .Lsds_dma_done
	s_mov_b32 m0, s28
	s_nop 0
	global_load_lds_dwordx4 v[254:255], off
.Lsds_dma_done:
	s_load_dwordx4 s[8:11], s[0:1], 0x0
	s_and_b32 s16, s2, 7
	s_bfe_u32 s14, s2, 0x10003
	s_cmp_eq_u32 s14, 0
	s_cselect_b64 s[12:13], -1, 0
	s_and_b64 s[4:5], s[12:13], exec
	s_mul_i32 s3, s16, 0x9600
	v_and_b32_e32 v206, 15, v0
	v_bfe_u32 v207, v0, 6, 2
	s_waitcnt lgkmcnt(0)
	s_cselect_b32 s4, s9, s11
	s_cselect_b32 s5, s8, s10
	s_lshl_b32 s3, s3, 2
	v_bfe_u32 v208, v0, 4, 2
	v_lshl_or_b32 v1, v207, 5, v206
	s_add_u32 s6, s5, s3
	v_lshlrev_b32_e32 v209, 3, v208
	v_mul_u32_u24_e32 v76, 0x12c, v1
	s_addc_u32 s7, s4, 0
	v_add_lshl_u32 v202, v209, v76, 2
	global_load_dwordx4 v[66:69], v202, s[6:7] offset:16
	global_load_dwordx4 v[70:73], v202, s[6:7]
	global_load_dwordx4 v[58:61], v202, s[6:7] offset:144
	global_load_dwordx4 v[62:65], v202, s[6:7] offset:128
	global_load_dwordx4 v[50:53], v202, s[6:7] offset:272
	global_load_dwordx4 v[54:57], v202, s[6:7] offset:256
	global_load_dwordx4 v[42:45], v202, s[6:7] offset:400
	global_load_dwordx4 v[46:49], v202, s[6:7] offset:384
	global_load_dwordx4 v[34:37], v202, s[6:7] offset:528
	global_load_dwordx4 v[38:41], v202, s[6:7] offset:512
	global_load_dwordx4 v[26:29], v202, s[6:7] offset:656
	global_load_dwordx4 v[30:33], v202, s[6:7] offset:640
	global_load_dwordx4 v[18:21], v202, s[6:7] offset:784
	global_load_dwordx4 v[22:25], v202, s[6:7] offset:768
	global_load_dwordx4 v[10:13], v202, s[6:7] offset:912
	global_load_dwordx4 v[14:17], v202, s[6:7] offset:896
	global_load_dwordx4 v[2:5], v202, s[6:7] offset:1040
	global_load_dwordx4 v[6:9], v202, s[6:7] offset:1024
	s_movk_i32 s8, 0x12c
	v_mov_b32_e32 v203, 0
	v_or_b32_e32 v1, 0x120, v209
	v_lshl_add_u64 v[74:75], s[6:7], 0, v[202:203]
	v_cmp_gt_u32_e32 vcc, s8, v1
	v_mov_b32_e32 v210, 0
	v_mov_b32_e32 v211, 0
	v_mov_b32_e32 v212, 0
	s_and_saveexec_b64 s[4:5], vcc
	s_cbranch_execz .LBB1_2
	global_load_dwordx4 v[78:81], v[74:75], off offset:1152
	s_waitcnt vmcnt(0)
	v_cvt_f16_f32_e32 v210, v78
	v_cvt_f16_f32_e32 v211, v81
	v_cvt_pk_f16_f32 v212, v79, v80

.LBB1_8:
	s_or_b64 exec, exec, s[6:7]
	s_waitcnt lgkmcnt(0)
	s_load_dwordx2 s[8:9], s[0:1], 0x18
	s_load_dwordx4 s[4:7], s[0:1], 0x28
	s_ashr_i32 s0, s2, 1
	s_and_b32 s17, s0, -8
	s_movk_i32 s0, 0x280
	v_cmp_gt_u32_e32 vcc, s0, v0
	s_and_saveexec_b64 s[0:1], vcc
	s_cbranch_execz .LBB1_21
	s_add_u32 s2, s10, s3
	s_addc_u32 s3, s11, 0
	s_mov_b64 s[10:11], 0
	s_movk_i32 s18, 0xffb0
	s_movk_i32 s19, 0x4b
	s_movk_i32 s20, 0x12c
	s_mov_b32 s21, 0x5040100
	s_mov_b32 s22, 0x1c400
	s_movk_i32 s23, 0x7f
	v_mov_b32_e32 v147, v0
	s_branch .LBB1_19

.LBB1_25:
	s_or_b64 exec, exec, s[0:1]
	v_cvt_f16_f32_e32 v85, v85
	v_cvt_f16_f32_e32 v78, v78
	v_cvt_f16_f32_e32 v6, v6
	v_cvt_pk_f16_f32 v87, v87, v88
	v_cvt_pk_f16_f32 v88, v83, v84
	v_cvt_pk_f16_f32 v84, v89, v82
	v_cvt_pk_f16_f32 v15, v15, v16
	v_cvt_pk_f16_f32 v11, v11, v12
	v_cvt_pk_f16_f32 v10, v17, v10
	v_lshrrev_b32_e32 v151, 8, v0
	v_alignbit_b32 v83, v84, v87, 16
	v_alignbit_b32 v84, v88, v84, 16
	v_alignbit_b32 v85, v85, v88, 16
	v_cvt_pk_f16_f32 v79, v79, v80
	v_cvt_pk_f16_f32 v80, v75, v76
	v_cvt_pk_f16_f32 v76, v81, v74
	v_alignbit_b32 v88, v10, v15, 16
	v_alignbit_b32 v89, v11, v10, 16
	v_cvt_pk_f16_f32 v7, v7, v8
	v_cvt_pk_f16_f32 v10, v3, v4
	v_cvt_pk_f16_f32 v2, v9, v2
	v_pack_b32_f16 v74, v78, v79
	v_alignbit_b32 v75, v76, v79, 16
	v_alignbit_b32 v78, v2, v7, 16
	v_alignbit_b32 v79, v10, v2, 16
	v_mul_u32_u24_e32 v2, 0x140, v151
	v_cvt_pk_f16_f32 v66, v73, v66
	v_pack_b32_f16 v73, v6, v7
	v_lshl_or_b32 v7, v208, 4, v2
	v_or_b32_e32 v2, 0x1d800, v7
	v_cvt_f16_f32_e32 v8, v5
	s_waitcnt vmcnt(0) lgkmcnt(0)
	s_barrier
	ds_read_b128 v[2:5], v2
	v_cvt_f16_f32_e32 v94, v94
	v_cvt_f16_f32_e32 v77, v77
	v_cvt_f16_f32_e32 v13, v13
	v_cvt_f16_f32_e32 v142, v142
	v_cvt_f16_f32_e32 v141, v141
	v_cvt_f16_f32_e32 v70, v70
	v_cvt_f16_f32_e32 v86, v86
	v_cvt_f16_f32_e32 v14, v14
	v_lshlrev_b32_e32 v6, 1, v209
	v_cvt_pk_f16_f32 v95, v95, v96
	v_or_b32_e32 v81, 0x1c400, v6
	v_cvt_pk_f16_f32 v143, v143, v144
	v_cvt_pk_f16_f32 v144, v139, v140
	v_cvt_pk_f16_f32 v140, v145, v138
	v_cvt_pk_f16_f32 v96, v91, v92
	v_cvt_pk_f16_f32 v92, v97, v90
	v_pack_b32_f16 v90, v94, v95
	v_alignbit_b32 v76, v80, v76, 16
	v_alignbit_b32 v77, v77, v80, 16
	v_cvt_pk_f16_f32 v71, v71, v72
	v_alignbit_b32 v94, v13, v11, 16
	v_alignbit_b32 v80, v8, v10, 16
	ds_read_b128 v[8:11], v81
	s_waitcnt lgkmcnt(1)
	v_add_f32_e32 v12, 0, v2
	v_pack_b32_f16 v138, v142, v143
	v_alignbit_b32 v139, v140, v143, 16
	v_alignbit_b32 v140, v144, v140, 16
	v_alignbit_b32 v141, v141, v144, 16
	v_pack_b32_f16 v143, v70, v71
	v_alignbit_b32 v144, v66, v71, 16
	v_mul_f32_e32 v71, -2.0, v2
	v_add_f32_e32 v2, v12, v3
	v_mul_f32_e32 v72, -2.0, v3
	v_add_u32_e32 v3, 0x1d840, v7
	v_pack_b32_f16 v82, v86, v87
	v_cvt_f16_f32_e32 v69, v69
	v_pack_b32_f16 v87, v14, v15
	ds_read_b128 v[12:15], v3
	v_add_f32_e32 v2, v2, v4
	v_cvt_pk_f16_f32 v67, v67, v68
	v_add_f32_e32 v16, v2, v5
	v_add_u32_e32 v2, 0x1d880, v7
	v_alignbit_b32 v150, v69, v67, 16
	v_mul_f32_e32 v69, -2.0, v4
	v_mul_f32_e32 v70, -2.0, v5
	ds_read_b128 v[2:5], v2
	s_waitcnt lgkmcnt(1)
	v_add_f32_e32 v16, v16, v12
	v_cvt_f16_f32_e32 v134, v134
	v_cvt_f16_f32_e32 v133, v133
	v_alignbit_b32 v145, v67, v66, 16
	v_cvt_f16_f32_e32 v62, v62
	v_mul_f32_e32 v67, -2.0, v12
	v_add_f32_e32 v12, v16, v13
	v_add_f32_e32 v12, v12, v14
	v_add_f32_e32 v12, v12, v15
	v_cvt_pk_f16_f32 v135, v135, v136
	v_cvt_pk_f16_f32 v136, v131, v132
	v_cvt_pk_f16_f32 v132, v137, v130
	v_cvt_pk_f16_f32 v63, v63, v64
	v_cvt_pk_f16_f32 v58, v65, v58
	s_waitcnt lgkmcnt(0)
	v_add_f32_e32 v12, v12, v2
	v_pack_b32_f16 v130, v134, v135
	v_alignbit_b32 v131, v132, v135, 16
	v_alignbit_b32 v132, v136, v132, 16
	v_alignbit_b32 v133, v133, v136, 16
	v_pack_b32_f16 v135, v62, v63
	v_alignbit_b32 v136, v58, v63, 16
	v_mul_f32_e32 v63, -2.0, v2
	v_add_f32_e32 v2, v12, v3
	v_mul_f32_e32 v64, -2.0, v3
	v_add_u32_e32 v3, 0x1d8c0, v7
	v_cvt_f16_f32_e32 v61, v61
	v_mul_f32_e32 v68, -2.0, v13
	v_mul_f32_e32 v65, -2.0, v14
	v_mul_f32_e32 v66, -2.0, v15
	ds_read_b128 v[12:15], v3
	v_add_f32_e32 v2, v2, v4
	v_cvt_pk_f16_f32 v59, v59, v60
	v_add_f32_e32 v16, v2, v5
	v_add_u32_e32 v2, 0x1d900, v7
	v_alignbit_b32 v142, v61, v59, 16
	v_mul_f32_e32 v61, -2.0, v4
	v_mul_f32_e32 v62, -2.0, v5
	ds_read_b128 v[2:5], v2
	s_waitcnt lgkmcnt(1)
	v_add_f32_e32 v7, v16, v12
	v_cvt_f16_f32_e32 v53, v53
	v_add_f32_e32 v7, v7, v13
	v_add_f32_e32 v7, v7, v14
	v_add_f32_e32 v7, v7, v15
	v_cvt_f16_f32_e32 v102, v102
	v_cvt_f16_f32_e32 v93, v93
	v_cvt_pk_f16_f32 v51, v51, v52
	v_cvt_f16_f32_e32 v21, v21
	s_waitcnt lgkmcnt(0)
	v_add_f32_e32 v7, v7, v2
	s_mov_b32 s0, 0x5040100
	v_alignbit_b32 v134, v53, v51, 16
	v_mul_f32_e32 v52, -2.0, v2
	v_add_f32_e32 v2, v7, v3
	v_mul_f32_e32 v53, -2.0, v3
	v_mul_u32_u24_e32 v3, 0x50, v151
	v_perm_b32 v146, v214, v204, s0
	v_perm_b32 v148, v212, v210, s0
	v_or_b32_e32 v3, v3, v206
	s_movk_i32 s0, 0x2a0
	v_cvt_pk_f16_f32 v103, v103, v104
	v_cvt_pk_f16_f32 v23, v23, v24
	v_cvt_pk_f16_f32 v19, v19, v20
	v_cvt_pk_f16_f32 v18, v25, v18
	v_mad_u32_u24 v86, v3, s0, v6
	v_cvt_f16_f32_e32 v126, v126
	v_cvt_pk_f16_f32 v104, v99, v100
	v_cvt_pk_f16_f32 v100, v105, v98
	v_pack_b32_f16 v98, v102, v103
	v_alignbit_b32 v91, v92, v95, 16
	v_alignbit_b32 v92, v96, v92, 16
	v_alignbit_b32 v93, v93, v96, 16
	v_alignbit_b32 v137, v59, v58, 16
	v_cvt_f16_f32_e32 v54, v54
	v_cvt_pk_f16_f32 v50, v57, v50
	v_alignbit_b32 v96, v18, v23, 16
	v_alignbit_b32 v97, v19, v18, 16
	v_alignbit_b32 v102, v21, v19, 16
	v_mul_f32_e32 v59, -2.0, v12
	v_mul_f32_e32 v60, -2.0, v13
	v_mul_f32_e32 v57, -2.0, v14
	v_mul_f32_e32 v58, -2.0, v15
	ds_read_b128 v[12:15], v86
	ds_read_b128 v[16:19], v86 offset:10752
	v_cvt_f16_f32_e32 v125, v125
	v_cvt_f16_f32_e32 v118, v118
	v_cvt_f16_f32_e32 v117, v117
	v_cvt_f16_f32_e32 v110, v110
	v_cvt_f16_f32_e32 v109, v109
	v_cvt_f16_f32_e32 v101, v101
	v_cvt_f16_f32_e32 v46, v46
	v_cvt_f16_f32_e32 v45, v45
	v_cvt_f16_f32_e32 v37, v37
	v_cvt_f16_f32_e32 v29, v29
	v_cvt_pk_f16_f32 v127, v127, v128
	v_cvt_pk_f16_f32 v128, v123, v124
	v_cvt_pk_f16_f32 v124, v129, v122
	v_cvt_pk_f16_f32 v55, v55, v56
	v_mov_b32_e32 v7, 0x1a400
	v_pack_b32_f16 v122, v126, v127
	v_alignbit_b32 v123, v124, v127, 16
	v_cvt_pk_f16_f32 v119, v119, v120
	v_cvt_pk_f16_f32 v120, v115, v116
	v_cvt_pk_f16_f32 v116, v121, v114
	v_cvt_pk_f16_f32 v111, v111, v112
	v_cvt_pk_f16_f32 v112, v107, v108
	v_cvt_pk_f16_f32 v108, v113, v106
	v_pack_b32_f16 v127, v54, v55
	v_cvt_pk_f16_f32 v47, v47, v48
	v_cvt_pk_f16_f32 v43, v43, v44
	v_cvt_pk_f16_f32 v42, v49, v42
	v_cvt_pk_f16_f32 v39, v39, v40
	v_cvt_pk_f16_f32 v35, v35, v36
	v_cvt_pk_f16_f32 v34, v41, v34
	v_cvt_pk_f16_f32 v31, v31, v32
	v_cvt_pk_f16_f32 v27, v27, v28
	v_cvt_pk_f16_f32 v26, v33, v26
	v_cvt_f16_f32_e32 v22, v22
	v_add_f32_e32 v2, v2, v4
	v_lshl_or_b32 v54, v151, 12, v7
	v_or_b32_e32 v7, 0x1c440, v6
	v_alignbit_b32 v124, v128, v124, 16
	v_alignbit_b32 v125, v125, v128, 16
	v_pack_b32_f16 v114, v118, v119
	v_alignbit_b32 v115, v116, v119, 16
	v_alignbit_b32 v116, v120, v116, 16
	v_alignbit_b32 v117, v117, v120, 16
	v_pack_b32_f16 v106, v110, v111
	v_alignbit_b32 v107, v108, v111, 16
	v_alignbit_b32 v108, v112, v108, 16
	v_alignbit_b32 v109, v109, v112, 16
	v_alignbit_b32 v99, v100, v103, 16
	v_alignbit_b32 v100, v104, v100, 16
	v_alignbit_b32 v101, v101, v104, 16
	v_alignbit_b32 v128, v50, v55, 16
	v_alignbit_b32 v129, v51, v50, 16
	v_pack_b32_f16 v119, v46, v47
	v_alignbit_b32 v120, v42, v47, 16
	v_alignbit_b32 v121, v43, v42, 16
	v_alignbit_b32 v126, v45, v43, 16
	v_cvt_f16_f32_e32 v38, v38
	v_alignbit_b32 v112, v34, v39, 16
	v_alignbit_b32 v113, v35, v34, 16
	v_alignbit_b32 v118, v37, v35, 16
	v_cvt_f16_f32_e32 v30, v30
	v_alignbit_b32 v104, v26, v31, 16
	v_alignbit_b32 v105, v27, v26, 16
	v_alignbit_b32 v110, v29, v27, 16
	v_mul_f32_e32 v51, -2.0, v4
	v_add_f32_e32 v50, v2, v5
	ds_read_b128 v[24:27], v86 offset:64
	v_mul_f32_e32 v56, -2.0, v5
	ds_read_b128 v[2:5], v86 offset:21504
	ds_read_b128 v[32:35], v86 offset:10816
	ds_read_b128 v[40:43], v86 offset:32256
	ds_read_b128 v[44:47], v86 offset:21568
	ds_read_b128 v[156:159], v7
	ds_read_b128 v[160:163], v86 offset:32320
	ds_read_b128 v[164:167], v86 offset:43008
	ds_read_b128 v[168:171], v86 offset:43072
	v_pack_b32_f16 v95, v22, v23
	v_pk_mul_f16 v22, v10, v145
	v_pk_mul_f16 v21, v9, v144
	v_pk_mul_f16 v23, v11, v150
	v_pk_mul_f16 v20, v8, v143
	v_pk_mul_f16 v10, v10, v140
	v_pk_mul_f16 v9, v9, v139
	v_pk_mul_f16 v11, v11, v141
	v_pk_mul_f16 v8, v8, v138
	v_or_b32_e32 v7, 0x1c480, v6
	v_pack_b32_f16 v111, v38, v39
	v_pack_b32_f16 v103, v30, v31
	s_waitcnt lgkmcnt(10)
	v_mfma_f32_16x16x32_f16 v[28:31], v[12:15], v[20:23], 0
	ds_read_b128 v[176:179], v7
	v_alignbit_b32 v147, v213, v214, 16
	v_alignbit_b32 v149, v211, v212, 16
	v_mfma_f32_16x16x32_f16 v[12:15], v[12:15], v[8:11], 0
	v_cmp_eq_u32_e32 vcc, 0, v208
	v_lshlrev_b32_e32 v55, 7, v207
	s_waitcnt lgkmcnt(4)
	v_pk_mul_f16 v182, v158, v137
	v_mfma_f32_16x16x32_f16 v[36:39], v[16:19], v[20:23], 0
	v_pk_mul_f16 v181, v157, v136
	v_pk_mul_f16 v183, v159, v142
	v_pk_mul_f16 v180, v156, v135
	v_mfma_f32_16x16x32_f16 v[16:19], v[16:19], v[8:11], 0
	v_pk_mul_f16 v158, v158, v132
	v_pk_mul_f16 v157, v157, v131
	v_pk_mul_f16 v159, v159, v133
	v_mfma_f32_16x16x32_f16 v[152:155], v[2:5], v[20:23], 0
	v_pk_mul_f16 v156, v156, v130
	v_mfma_f32_16x16x32_f16 v[2:5], v[2:5], v[8:11], 0
	v_mfma_f32_16x16x32_f16 v[172:175], v[40:43], v[20:23], 0
	v_mfma_f32_16x16x32_f16 v[40:43], v[40:43], v[8:11], 0
	s_waitcnt lgkmcnt(2)
	v_mfma_f32_16x16x32_f16 v[20:23], v[164:167], v[20:23], 0
	v_mfma_f32_16x16x32_f16 v[8:11], v[164:167], v[8:11], 0
	v_mfma_f32_16x16x32_f16 v[28:31], v[24:27], v[180:183], v[28:31]
	v_or_b32_e32 v7, 0x1c4c0, v6
	s_waitcnt lgkmcnt(0)
	v_pk_mul_f16 v186, v178, v129
	v_pk_mul_f16 v185, v177, v128
	v_mfma_f32_16x16x32_f16 v[12:15], v[24:27], v[156:159], v[12:15]
	v_pk_mul_f16 v187, v179, v134
	v_pk_mul_f16 v184, v176, v127
	v_pk_mul_f16 v178, v178, v124
	v_mfma_f32_16x16x32_f16 v[24:27], v[32:35], v[180:183], v[36:39]
	v_pk_mul_f16 v177, v177, v123
	v_pk_mul_f16 v179, v179, v125
	v_pk_mul_f16 v176, v176, v122
	v_mfma_f32_16x16x32_f16 v[16:19], v[32:35], v[156:159], v[16:19]
	v_mfma_f32_16x16x32_f16 v[32:35], v[44:47], v[180:183], v[152:155]
	ds_read_b128 v[36:39], v86 offset:10880
	s_nop 1
	ds_read_b128 v[152:155], v86 offset:21632
	v_mfma_f32_16x16x32_f16 v[2:5], v[44:47], v[156:159], v[2:5]
	ds_read_b128 v[44:47], v86 offset:128
	ds_read_b128 v[164:167], v86 offset:43136
	v_mfma_f32_16x16x32_f16 v[172:175], v[160:163], v[180:183], v[172:175]
	v_mfma_f32_16x16x32_f16 v[40:43], v[160:163], v[156:159], v[40:43]
	v_mfma_f32_16x16x32_f16 v[20:23], v[168:171], v[180:183], v[20:23]
	ds_read_b128 v[160:163], v86 offset:32384
	ds_read_b128 v[180:183], v7
	v_mfma_f32_16x16x32_f16 v[8:11], v[168:171], v[156:159], v[8:11]
	s_waitcnt lgkmcnt(3)
	v_mfma_f32_16x16x32_f16 v[28:31], v[44:47], v[184:187], v[28:31]
	v_or_b32_e32 v7, 0x1c500, v6
	s_waitcnt lgkmcnt(0)
	v_pk_mul_f16 v170, v182, v121
	v_pk_mul_f16 v169, v181, v120
	v_mfma_f32_16x16x32_f16 v[12:15], v[44:47], v[176:179], v[12:15]
	v_pk_mul_f16 v171, v183, v126
	v_pk_mul_f16 v168, v180, v119
	v_pk_mul_f16 v182, v182, v116
	v_mfma_f32_16x16x32_f16 v[24:27], v[36:39], v[184:187], v[24:27]
	v_pk_mul_f16 v181, v181, v115
	v_pk_mul_f16 v183, v183, v117
	v_pk_mul_f16 v180, v180, v114
	v_mfma_f32_16x16x32_f16 v[16:19], v[36:39], v[176:179], v[16:19]
	ds_read_b128 v[36:39], v86 offset:10944
	ds_read_b128 v[44:47], v86 offset:21696
	v_mfma_f32_16x16x32_f16 v[32:35], v[152:155], v[184:187], v[32:35]
	v_mfma_f32_16x16x32_f16 v[2:5], v[152:155], v[176:179], v[2:5]
	ds_read_b128 v[152:155], v86 offset:192
	ds_read_b128 v[156:159], v86 offset:43200
	v_mfma_f32_16x16x32_f16 v[172:175], v[160:163], v[184:187], v[172:175]
	v_mfma_f32_16x16x32_f16 v[40:43], v[160:163], v[176:179], v[40:43]
	v_mfma_f32_16x16x32_f16 v[20:23], v[164:167], v[184:187], v[20:23]
	ds_read_b128 v[160:163], v86 offset:32448
	ds_read_b128 v[184:187], v7
	v_mfma_f32_16x16x32_f16 v[8:11], v[164:167], v[176:179], v[8:11]
	s_waitcnt lgkmcnt(3)
	v_mfma_f32_16x16x32_f16 v[28:31], v[152:155], v[168:171], v[28:31]
	v_or_b32_e32 v7, 0x1c540, v6
	s_waitcnt lgkmcnt(0)
	v_pk_mul_f16 v178, v186, v113
	v_pk_mul_f16 v177, v185, v112
	v_mfma_f32_16x16x32_f16 v[12:15], v[152:155], v[180:183], v[12:15]
	v_pk_mul_f16 v179, v187, v118
	v_pk_mul_f16 v176, v184, v111
	v_pk_mul_f16 v186, v186, v108
	v_mfma_f32_16x16x32_f16 v[24:27], v[36:39], v[168:171], v[24:27]
	v_pk_mul_f16 v185, v185, v107
	v_pk_mul_f16 v187, v187, v109
	v_pk_mul_f16 v184, v184, v106
	v_mfma_f32_16x16x32_f16 v[16:19], v[36:39], v[180:183], v[16:19]
	ds_read_b128 v[36:39], v86 offset:11008
	ds_read_b128 v[152:155], v86 offset:21760
	v_mfma_f32_16x16x32_f16 v[32:35], v[44:47], v[168:171], v[32:35]
	v_mfma_f32_16x16x32_f16 v[2:5], v[44:47], v[180:183], v[2:5]
	ds_read_b128 v[44:47], v86 offset:256
	ds_read_b128 v[164:167], v86 offset:43264
	v_mfma_f32_16x16x32_f16 v[172:175], v[160:163], v[168:171], v[172:175]
	v_mfma_f32_16x16x32_f16 v[40:43], v[160:163], v[180:183], v[40:43]
	v_mfma_f32_16x16x32_f16 v[20:23], v[156:159], v[168:171], v[20:23]
	ds_read_b128 v[160:163], v86 offset:32512
	ds_read_b128 v[168:171], v7
	v_mfma_f32_16x16x32_f16 v[8:11], v[156:159], v[180:183], v[8:11]
	s_waitcnt lgkmcnt(3)
	v_mfma_f32_16x16x32_f16 v[28:31], v[44:47], v[176:179], v[28:31]
	v_or_b32_e32 v7, 0x1c580, v6
	s_waitcnt lgkmcnt(0)
	v_pk_mul_f16 v182, v170, v105
	v_pk_mul_f16 v181, v169, v104
	v_mfma_f32_16x16x32_f16 v[12:15], v[44:47], v[184:187], v[12:15]
	v_pk_mul_f16 v183, v171, v110
	v_pk_mul_f16 v180, v168, v103
	v_pk_mul_f16 v170, v170, v100
	v_mfma_f32_16x16x32_f16 v[24:27], v[36:39], v[176:179], v[24:27]
	v_pk_mul_f16 v169, v169, v99
	v_pk_mul_f16 v171, v171, v101
	v_pk_mul_f16 v168, v168, v98
	v_mfma_f32_16x16x32_f16 v[16:19], v[36:39], v[184:187], v[16:19]
	ds_read_b128 v[36:39], v86 offset:11072
	ds_read_b128 v[44:47], v86 offset:21824
	v_mfma_f32_16x16x32_f16 v[32:35], v[152:155], v[176:179], v[32:35]
	v_mfma_f32_16x16x32_f16 v[2:5], v[152:155], v[184:187], v[2:5]
	ds_read_b128 v[152:155], v86 offset:320
	ds_read_b128 v[156:159], v86 offset:43328
	v_mfma_f32_16x16x32_f16 v[172:175], v[160:163], v[176:179], v[172:175]
	v_mfma_f32_16x16x32_f16 v[40:43], v[160:163], v[184:187], v[40:43]
	v_mfma_f32_16x16x32_f16 v[20:23], v[164:167], v[176:179], v[20:23]
	ds_read_b128 v[160:163], v86 offset:32576
	ds_read_b128 v[176:179], v7
	v_mfma_f32_16x16x32_f16 v[8:11], v[164:167], v[184:187], v[8:11]
	s_waitcnt lgkmcnt(3)
	v_mfma_f32_16x16x32_f16 v[28:31], v[152:155], v[180:183], v[28:31]
	v_or_b32_e32 v7, 0x1c5c0, v6
	s_waitcnt lgkmcnt(0)
	v_pk_mul_f16 v186, v178, v97
	v_pk_mul_f16 v185, v177, v96
	v_mfma_f32_16x16x32_f16 v[12:15], v[152:155], v[168:171], v[12:15]
	v_pk_mul_f16 v187, v179, v102
	v_pk_mul_f16 v184, v176, v95
	v_pk_mul_f16 v178, v178, v92
	v_mfma_f32_16x16x32_f16 v[24:27], v[36:39], v[180:183], v[24:27]
	v_pk_mul_f16 v177, v177, v91
	v_pk_mul_f16 v179, v179, v93
	v_pk_mul_f16 v176, v176, v90
	v_mfma_f32_16x16x32_f16 v[16:19], v[36:39], v[168:171], v[16:19]
	ds_read_b128 v[36:39], v86 offset:11136
	ds_read_b128 v[152:155], v86 offset:21888
	v_mfma_f32_16x16x32_f16 v[32:35], v[44:47], v[180:183], v[32:35]
	v_mfma_f32_16x16x32_f16 v[2:5], v[44:47], v[168:171], v[2:5]
	ds_read_b128 v[44:47], v86 offset:384
	ds_read_b128 v[164:167], v86 offset:43392
	v_mfma_f32_16x16x32_f16 v[172:175], v[160:163], v[180:183], v[172:175]
	v_mfma_f32_16x16x32_f16 v[40:43], v[160:163], v[168:171], v[40:43]
	v_mfma_f32_16x16x32_f16 v[20:23], v[156:159], v[180:183], v[20:23]
	ds_read_b128 v[160:163], v86 offset:32640
	ds_read_b128 v[180:183], v7
	v_mfma_f32_16x16x32_f16 v[8:11], v[156:159], v[168:171], v[8:11]
	s_waitcnt lgkmcnt(3)
	v_mfma_f32_16x16x32_f16 v[28:31], v[44:47], v[184:187], v[28:31]
	v_or_b32_e32 v7, 0x1c600, v6
	s_waitcnt lgkmcnt(0)
	v_pk_mul_f16 v170, v182, v89
	v_pk_mul_f16 v169, v181, v88
	v_mfma_f32_16x16x32_f16 v[12:15], v[44:47], v[176:179], v[12:15]
	v_pk_mul_f16 v171, v183, v94
	v_pk_mul_f16 v168, v180, v87
	v_pk_mul_f16 v182, v182, v84
	v_mfma_f32_16x16x32_f16 v[24:27], v[36:39], v[184:187], v[24:27]
	v_pk_mul_f16 v181, v181, v83
	v_pk_mul_f16 v183, v183, v85
	v_pk_mul_f16 v180, v180, v82
	v_mfma_f32_16x16x32_f16 v[16:19], v[36:39], v[176:179], v[16:19]
	ds_read_b128 v[36:39], v86 offset:11200
	ds_read_b128 v[44:47], v86 offset:21952
	v_mfma_f32_16x16x32_f16 v[32:35], v[152:155], v[184:187], v[32:35]
	v_mfma_f32_16x16x32_f16 v[2:5], v[152:155], v[176:179], v[2:5]
	ds_read_b128 v[152:155], v86 offset:448
	ds_read_b128 v[156:159], v86 offset:43456
	v_mfma_f32_16x16x32_f16 v[172:175], v[160:163], v[184:187], v[172:175]
	v_mfma_f32_16x16x32_f16 v[40:43], v[160:163], v[176:179], v[40:43]
	v_mfma_f32_16x16x32_f16 v[20:23], v[164:167], v[184:187], v[20:23]
	ds_read_b128 v[160:163], v86 offset:32704
	ds_read_b128 v[184:187], v7
	v_mfma_f32_16x16x32_f16 v[8:11], v[164:167], v[176:179], v[8:11]
	s_waitcnt lgkmcnt(3)
	v_mfma_f32_16x16x32_f16 v[28:31], v[152:155], v[168:171], v[28:31]
	v_or_b32_e32 v7, 0x1c640, v6
	s_waitcnt lgkmcnt(0)
	v_pk_mul_f16 v178, v186, v79
	v_pk_mul_f16 v177, v185, v78
	v_mfma_f32_16x16x32_f16 v[12:15], v[152:155], v[180:183], v[12:15]
	v_pk_mul_f16 v179, v187, v80
	v_pk_mul_f16 v176, v184, v73
	v_pk_mul_f16 v186, v186, v76
	v_mfma_f32_16x16x32_f16 v[24:27], v[36:39], v[168:171], v[24:27]
	v_pk_mul_f16 v185, v185, v75
	v_pk_mul_f16 v187, v187, v77
	v_pk_mul_f16 v184, v184, v74
	v_mfma_f32_16x16x32_f16 v[16:19], v[36:39], v[180:183], v[16:19]
	ds_read_b128 v[36:39], v86 offset:512
	ds_read_b128 v[152:155], v86 offset:11264
	v_mfma_f32_16x16x32_f16 v[32:35], v[44:47], v[168:171], v[32:35]
	v_mfma_f32_16x16x32_f16 v[2:5], v[44:47], v[180:183], v[2:5]
	ds_read_b128 v[44:47], v86 offset:32768
	ds_read_b128 v[164:167], v86 offset:43520
	v_mfma_f32_16x16x32_f16 v[172:175], v[160:163], v[168:171], v[172:175]
	v_mfma_f32_16x16x32_f16 v[40:43], v[160:163], v[180:183], v[40:43]
	v_mfma_f32_16x16x32_f16 v[20:23], v[156:159], v[168:171], v[20:23]
	ds_read_b128 v[160:163], v86 offset:22016
	ds_read_b128 v[168:171], v7
	v_mfma_f32_16x16x32_f16 v[8:11], v[156:159], v[180:183], v[8:11]
	s_waitcnt lgkmcnt(5)
	v_mfma_f32_16x16x32_f16 v[28:31], v[36:39], v[176:179], v[28:31]
	s_waitcnt lgkmcnt(0)
	v_pk_mul_f16 v189, v169, v149
	v_pk_mul_f16 v188, v168, v148
	v_pk_mul_f16 v191, v171, v1
	v_mfma_f32_16x16x32_f16 v[12:15], v[36:39], v[184:187], v[12:15]
	v_pk_mul_f16 v190, v170, v203
	v_mfma_f32_16x16x32_f16 v[24:27], v[152:155], v[176:179], v[24:27]
	v_mfma_f32_16x16x32_f16 v[16:19], v[152:155], v[184:187], v[16:19]
	v_mfma_f32_16x16x32_f16 v[36:39], v[160:163], v[176:179], v[32:35]
	s_nop 2
	ds_read_b128 v[32:35], v86 offset:576
	ds_read_b128 v[152:155], v86 offset:11328
	ds_read_b128 v[156:159], v86 offset:22080
	v_mfma_f32_16x16x32_f16 v[2:5], v[160:163], v[184:187], v[2:5]
	v_mfma_f32_16x16x32_f16 v[160:163], v[44:47], v[176:179], v[172:175]
	s_nop 2
	ds_read_b128 v[172:175], v86 offset:32832
	ds_read_b128 v[180:183], v86 offset:43584
	v_mfma_f32_16x16x32_f16 v[40:43], v[44:47], v[184:187], v[40:43]
	v_pk_mul_f16 v45, v169, v147
	v_pk_mul_f16 v44, v168, v146
	v_pk_mul_f16 v47, v171, v202
	v_mfma_f32_16x16x32_f16 v[8:11], v[164:167], v[184:187], v[8:11]
	v_pk_mul_f16 v46, v170, v205
	v_mfma_f32_16x16x32_f16 v[176:179], v[164:167], v[176:179], v[20:23]
	s_waitcnt lgkmcnt(4)
	v_mfma_f32_16x16x32_f16 v[164:167], v[32:35], v[188:191], v[28:31]
	v_mfma_f32_16x16x32_f16 v[168:171], v[32:35], v[44:47], v[12:15]
	s_waitcnt lgkmcnt(3)
	v_mfma_f32_16x16x32_f16 v[28:31], v[152:155], v[188:191], v[24:27]
	v_mfma_f32_16x16x32_f16 v[32:35], v[152:155], v[44:47], v[16:19]
	s_waitcnt lgkmcnt(2)
	v_mfma_f32_16x16x32_f16 v[20:23], v[156:159], v[188:191], v[36:39]
	v_mfma_f32_16x16x32_f16 v[24:27], v[156:159], v[44:47], v[2:5]
	s_waitcnt lgkmcnt(1)
	v_mfma_f32_16x16x32_f16 v[2:5], v[172:175], v[188:191], v[160:163]
	v_mfma_f32_16x16x32_f16 v[16:19], v[172:175], v[44:47], v[40:43]
	s_waitcnt lgkmcnt(0)
	v_mfma_f32_16x16x32_f16 v[12:15], v[180:183], v[188:191], v[176:179]
	v_mfma_f32_16x16x32_f16 v[8:11], v[180:183], v[44:47], v[8:11]
	v_or_b32_e32 v7, 0x1c680, v6
	ds_read_b128 v[36:39], v7
	ds_read_b128 v[40:43], v86
	v_or_b32_e32 v7, 0x1c6c0, v6
	ds_read_b128 v[44:47], v7
	ds_read_b128 v[156:159], v86 offset:64
	v_or_b32_e32 v7, 0x1c700, v6
	v_exp_f32_e32 v48, v168
	v_exp_f32_e32 v49, v164
	ds_read_b128 v[172:175], v86 offset:10752
	ds_read_b128 v[176:179], v86 offset:10816
	ds_read_b128 v[184:187], v86 offset:21504
	ds_read_b128 v[188:191], v86 offset:21568
	ds_read_b128 v[196:199], v86 offset:32256
	ds_read_b128 v[208:211], v86 offset:32320
	ds_read_b128 v[212:215], v86 offset:43008
	ds_read_b128 v[216:219], v86 offset:43072
	ds_read_b128 v[228:231], v7
	v_exp_f32_e32 v7, v169
	v_exp_f32_e32 v151, v165
	v_add_f32_e32 v48, 1.0, v48
	v_add_f32_e32 v49, 1.0, v49
	s_waitcnt lgkmcnt(12)
	v_pk_mul_f16 v154, v38, v145
	v_pk_mul_f16 v153, v37, v144
	v_pk_mul_f16 v155, v39, v150
	v_pk_mul_f16 v152, v36, v143
	v_pk_mul_f16 v38, v38, v140
	v_pk_mul_f16 v37, v37, v139
	v_pk_mul_f16 v39, v39, v141
	v_pk_mul_f16 v36, v36, v138
	v_rcp_f32_e32 v48, v48
	v_add_f32_e32 v7, 1.0, v7
	v_rcp_f32_e32 v49, v49
	v_add_f32_e32 v151, 1.0, v151
	s_waitcnt lgkmcnt(11)
	v_mfma_f32_16x16x32_f16 v[160:163], v[40:43], v[152:155], 0
	v_rcp_f32_e32 v7, v7
	v_rcp_f32_e32 v151, v151
	s_waitcnt lgkmcnt(10)
	v_pk_mul_f16 v222, v46, v137
	v_mfma_f32_16x16x32_f16 v[40:43], v[40:43], v[36:39], 0
	v_pk_mul_f16 v221, v45, v136
	v_pk_mul_f16 v223, v47, v142
	v_pk_mul_f16 v220, v44, v135
	s_waitcnt lgkmcnt(8)
	v_mfma_f32_16x16x32_f16 v[180:183], v[172:175], v[152:155], 0
	v_pk_mul_f16 v46, v46, v132
	v_pk_mul_f16 v45, v45, v131
	v_pk_mul_f16 v47, v47, v133
	v_mfma_f32_16x16x32_f16 v[172:175], v[172:175], v[36:39], 0
	v_pk_mul_f16 v44, v44, v130
	v_fma_f32 v48, v71, v48, v50
	v_fma_f32 v49, v71, v49, v50
	s_waitcnt lgkmcnt(6)
	v_mfma_f32_16x16x32_f16 v[192:195], v[184:187], v[152:155], 0
	v_fmac_f32_e32 v48, v72, v7
	v_fmac_f32_e32 v49, v72, v151
	v_mfma_f32_16x16x32_f16 v[184:187], v[184:187], v[36:39], 0
	s_waitcnt lgkmcnt(4)
	v_mfma_f32_16x16x32_f16 v[224:227], v[196:199], v[152:155], 0
	v_mfma_f32_16x16x32_f16 v[196:199], v[196:199], v[36:39], 0
	s_waitcnt lgkmcnt(2)
	v_mfma_f32_16x16x32_f16 v[152:155], v[212:215], v[152:155], 0
	v_mfma_f32_16x16x32_f16 v[36:39], v[212:215], v[36:39], 0
	v_or_b32_e32 v7, 0x1c740, v6
	v_exp_f32_e32 v151, v170
	ds_read_b128 v[212:215], v86 offset:10880
	ds_read_b128 v[232:235], v86 offset:21632
	v_mfma_f32_16x16x32_f16 v[160:163], v[156:159], v[220:223], v[160:163]
	ds_read_b128 v[236:239], v86 offset:128
	ds_read_b128 v[240:243], v86 offset:43136
	s_waitcnt lgkmcnt(4)
	v_pk_mul_f16 v246, v230, v129
	v_pk_mul_f16 v245, v229, v128
	v_mfma_f32_16x16x32_f16 v[40:43], v[156:159], v[44:47], v[40:43]
	v_pk_mul_f16 v247, v231, v134
	v_pk_mul_f16 v244, v228, v127
	v_add_f32_e32 v151, 1.0, v151
	v_mfma_f32_16x16x32_f16 v[156:159], v[176:179], v[220:223], v[180:183]
	v_rcp_f32_e32 v151, v151
	s_nop 0
	v_fmac_f32_e32 v48, v69, v151
	v_pk_mul_f16 v182, v230, v124
	v_pk_mul_f16 v181, v229, v123
	v_pk_mul_f16 v183, v231, v125
	v_mfma_f32_16x16x32_f16 v[172:175], v[176:179], v[44:47], v[172:175]
	v_pk_mul_f16 v180, v228, v122
	v_exp_f32_e32 v151, v166
	v_mfma_f32_16x16x32_f16 v[176:179], v[188:191], v[220:223], v[192:195]
	s_nop 2
	ds_read_b128 v[192:195], v86 offset:32384
	ds_read_b128 v[228:231], v7
	v_exp_f32_e32 v7, v171
	v_add_f32_e32 v151, 1.0, v151
	v_rcp_f32_e32 v151, v151
	v_mfma_f32_16x16x32_f16 v[152:155], v[216:219], v[220:223], v[152:155]
	v_add_f32_e32 v7, 1.0, v7
	v_rcp_f32_e32 v7, v7
	v_fmac_f32_e32 v49, v69, v151
	v_mfma_f32_16x16x32_f16 v[36:39], v[216:219], v[44:47], v[36:39]
	v_fmac_f32_e32 v48, v70, v7
	v_exp_f32_e32 v7, v167
	v_mfma_f32_16x16x32_f16 v[168:171], v[188:191], v[44:47], v[184:187]
	v_add_f32_e32 v7, 1.0, v7
	v_rcp_f32_e32 v7, v7
	v_mfma_f32_16x16x32_f16 v[184:187], v[208:211], v[220:223], v[224:227]
	v_fmac_f32_e32 v49, v70, v7
	v_mfma_f32_16x16x32_f16 v[188:191], v[208:211], v[44:47], v[196:199]
	v_or_b32_e32 v7, 0x1c780, v6
	v_exp_f32_e32 v32, v32
	ds_read_b128 v[44:47], v86 offset:10944
	ds_read_b128 v[164:167], v86 offset:21696
	ds_read_b128 v[196:199], v86 offset:192
	ds_read_b128 v[208:211], v86 offset:43200
	s_waitcnt lgkmcnt(9)
	v_mfma_f32_16x16x32_f16 v[156:159], v[212:215], v[244:247], v[156:159]
	v_add_f32_e32 v32, 1.0, v32
	v_rcp_f32_e32 v32, v32
	v_exp_f32_e32 v28, v28
	v_mfma_f32_16x16x32_f16 v[172:175], v[212:215], v[180:183], v[172:175]
	ds_read_b128 v[212:215], v86 offset:32448
	ds_read_b128 v[224:227], v7
	v_exp_f32_e32 v7, v33
	v_fmac_f32_e32 v48, v67, v32
	v_add_f32_e32 v28, 1.0, v28
	v_rcp_f32_e32 v28, v28
	v_add_f32_e32 v7, 1.0, v7
	v_rcp_f32_e32 v7, v7
	s_waitcnt lgkmcnt(9)
	v_mfma_f32_16x16x32_f16 v[40:43], v[236:239], v[180:183], v[40:43]
	v_fmac_f32_e32 v49, v67, v28
	s_waitcnt lgkmcnt(6)
	v_pk_mul_f16 v218, v230, v121
	v_fmac_f32_e32 v48, v68, v7
	v_exp_f32_e32 v7, v29
	v_mfma_f32_16x16x32_f16 v[152:155], v[240:243], v[244:247], v[152:155]
	v_pk_mul_f16 v217, v229, v120
	v_pk_mul_f16 v219, v231, v126
	v_add_f32_e32 v7, 1.0, v7
	v_rcp_f32_e32 v7, v7
	v_mfma_f32_16x16x32_f16 v[36:39], v[240:243], v[180:183], v[36:39]
	v_pk_mul_f16 v216, v228, v119
	v_pk_mul_f16 v222, v230, v116
	v_pk_mul_f16 v221, v229, v115
	v_mfma_f32_16x16x32_f16 v[160:163], v[236:239], v[244:247], v[160:163]
	v_pk_mul_f16 v223, v231, v117
	v_pk_mul_f16 v220, v228, v114
	v_fmac_f32_e32 v49, v68, v7
	v_mfma_f32_16x16x32_f16 v[176:179], v[232:235], v[244:247], v[176:179]
	v_mfma_f32_16x16x32_f16 v[168:171], v[232:235], v[180:183], v[168:171]
	v_mfma_f32_16x16x32_f16 v[184:187], v[192:195], v[244:247], v[184:187]
	v_mfma_f32_16x16x32_f16 v[188:191], v[192:195], v[180:183], v[188:191]
	v_or_b32_e32 v7, 0x1c7c0, v6
	v_exp_f32_e32 v28, v34
	ds_read_b128 v[180:183], v86 offset:11008
	ds_read_b128 v[192:195], v86 offset:21760
	ds_read_b128 v[228:231], v86 offset:256
	ds_read_b128 v[232:235], v86 offset:43264
	s_waitcnt lgkmcnt(9)
	v_mfma_f32_16x16x32_f16 v[156:159], v[44:47], v[216:219], v[156:159]
	v_add_f32_e32 v28, 1.0, v28
	v_rcp_f32_e32 v28, v28
	s_waitcnt lgkmcnt(4)
	v_pk_mul_f16 v200, v226, v113
	v_mfma_f32_16x16x32_f16 v[44:47], v[44:47], v[220:223], v[172:175]
	v_pk_mul_f16 v201, v227, v118
	v_fmac_f32_e32 v48, v65, v28
	v_exp_f32_e32 v28, v30
	v_mfma_f32_16x16x32_f16 v[172:175], v[164:167], v[216:219], v[176:179]
	s_nop 2
	ds_read_b128 v[176:179], v86 offset:32512
	ds_read_b128 v[236:239], v7
	v_exp_f32_e32 v7, v35
	v_add_f32_e32 v151, 1.0, v28
	v_rcp_f32_e32 v151, v151
	v_mfma_f32_16x16x32_f16 v[40:43], v[196:199], v[220:223], v[40:43]
	v_add_f32_e32 v7, 1.0, v7
	v_rcp_f32_e32 v7, v7
	v_fmac_f32_e32 v49, v65, v151
	v_mfma_f32_16x16x32_f16 v[32:35], v[164:167], v[220:223], v[168:171]
	v_pk_mul_f16 v226, v226, v108
	v_fmac_f32_e32 v48, v66, v7
	v_exp_f32_e32 v7, v31
	v_mfma_f32_16x16x32_f16 v[28:31], v[208:211], v[216:219], v[152:155]
	v_pk_mul_f16 v227, v227, v109
	v_add_f32_e32 v7, 1.0, v7
	v_rcp_f32_e32 v7, v7
	v_mfma_f32_16x16x32_f16 v[36:39], v[208:211], v[220:223], v[36:39]
	v_fmac_f32_e32 v49, v66, v7
	v_mfma_f32_16x16x32_f16 v[160:163], v[196:199], v[216:219], v[160:163]
	v_pk_mul_f16 v199, v225, v112
	v_pk_mul_f16 v198, v224, v111
	v_pk_mul_f16 v225, v225, v107
	v_pk_mul_f16 v224, v224, v106
	v_mfma_f32_16x16x32_f16 v[164:167], v[212:215], v[216:219], v[184:187]
	v_mfma_f32_16x16x32_f16 v[168:171], v[212:215], v[220:223], v[188:191]
	v_or_b32_e32 v7, 0x1c800, v6
	v_exp_f32_e32 v24, v24
	ds_read_b128 v[152:155], v86 offset:11072
	ds_read_b128 v[184:187], v86 offset:21824
	ds_read_b128 v[188:191], v86 offset:320
	ds_read_b128 v[208:211], v86 offset:43328
	s_waitcnt lgkmcnt(9)
	v_mfma_f32_16x16x32_f16 v[156:159], v[180:183], v[198:201], v[156:159]
	v_add_f32_e32 v24, 1.0, v24
	v_rcp_f32_e32 v24, v24
	v_exp_f32_e32 v20, v20
	v_mfma_f32_16x16x32_f16 v[44:47], v[180:183], v[224:227], v[44:47]
	ds_read_b128 v[180:183], v86 offset:32576
	ds_read_b128 v[220:223], v7
	v_exp_f32_e32 v7, v25
	v_fmac_f32_e32 v48, v63, v24
	v_add_f32_e32 v20, 1.0, v20
	v_rcp_f32_e32 v20, v20
	v_add_f32_e32 v7, 1.0, v7
	v_rcp_f32_e32 v7, v7
	s_waitcnt lgkmcnt(9)
	v_mfma_f32_16x16x32_f16 v[40:43], v[228:231], v[224:227], v[40:43]
	v_fmac_f32_e32 v49, v63, v20
	s_waitcnt lgkmcnt(6)
	v_pk_mul_f16 v214, v238, v105
	v_fmac_f32_e32 v48, v64, v7
	v_exp_f32_e32 v7, v21
	v_mfma_f32_16x16x32_f16 v[32:35], v[192:195], v[224:227], v[32:35]
	v_pk_mul_f16 v213, v237, v104
	v_pk_mul_f16 v215, v239, v110
	v_add_f32_e32 v7, 1.0, v7
	v_mfma_f32_16x16x32_f16 v[28:31], v[232:235], v[198:201], v[28:31]
	v_rcp_f32_e32 v7, v7
	v_pk_mul_f16 v212, v236, v103
	v_pk_mul_f16 v218, v238, v100
	v_mfma_f32_16x16x32_f16 v[36:39], v[232:235], v[224:227], v[36:39]
	v_pk_mul_f16 v217, v237, v99
	v_pk_mul_f16 v219, v239, v101
	v_pk_mul_f16 v216, v236, v98
	v_mfma_f32_16x16x32_f16 v[160:163], v[228:231], v[198:201], v[160:163]
	v_fmac_f32_e32 v49, v64, v7
	v_mfma_f32_16x16x32_f16 v[172:175], v[192:195], v[198:201], v[172:175]
	v_mfma_f32_16x16x32_f16 v[164:167], v[176:179], v[198:201], v[164:167]
	v_mfma_f32_16x16x32_f16 v[168:171], v[176:179], v[224:227], v[168:171]
	v_or_b32_e32 v7, 0x1c840, v6
	v_exp_f32_e32 v20, v26
	ds_read_b128 v[176:179], v86 offset:11136
	ds_read_b128 v[192:195], v86 offset:21888
	s_waitcnt lgkmcnt(5)
	v_mfma_f32_16x16x32_f16 v[160:163], v[188:191], v[212:215], v[160:163]
	ds_read_b128 v[196:199], v86 offset:384
	ds_read_b128 v[224:227], v86 offset:43392
	s_waitcnt lgkmcnt(4)
	v_pk_mul_f16 v230, v222, v97
	v_pk_mul_f16 v229, v221, v96
	v_mfma_f32_16x16x32_f16 v[40:43], v[188:191], v[216:219], v[40:43]
	v_pk_mul_f16 v231, v223, v102
	v_pk_mul_f16 v228, v220, v95
	v_pk_mul_f16 v190, v222, v92
	v_mfma_f32_16x16x32_f16 v[156:159], v[152:155], v[212:215], v[156:159]
	v_pk_mul_f16 v189, v221, v91
	v_pk_mul_f16 v191, v223, v93
	v_pk_mul_f16 v188, v220, v90
	v_mfma_f32_16x16x32_f16 v[44:47], v[152:155], v[216:219], v[44:47]
	v_add_f32_e32 v20, 1.0, v20
	v_rcp_f32_e32 v20, v20
	v_mfma_f32_16x16x32_f16 v[152:155], v[184:187], v[212:215], v[172:175]
	s_nop 2
	ds_read_b128 v[172:175], v86 offset:32640
	ds_read_b128 v[220:223], v7
	v_exp_f32_e32 v7, v27
	v_fmac_f32_e32 v48, v61, v20
	v_exp_f32_e32 v20, v22
	v_mfma_f32_16x16x32_f16 v[24:27], v[184:187], v[216:219], v[32:35]
	v_add_f32_e32 v7, 1.0, v7
	v_rcp_f32_e32 v7, v7
	v_add_f32_e32 v151, 1.0, v20
	v_rcp_f32_e32 v151, v151
	v_mfma_f32_16x16x32_f16 v[32:35], v[180:183], v[212:215], v[164:167]
	v_fmac_f32_e32 v48, v62, v7
	v_exp_f32_e32 v7, v23
	v_fmac_f32_e32 v49, v61, v151
	v_mfma_f32_16x16x32_f16 v[20:23], v[208:211], v[212:215], v[28:31]
	v_add_f32_e32 v7, 1.0, v7
	v_rcp_f32_e32 v7, v7
	v_mfma_f32_16x16x32_f16 v[28:31], v[208:211], v[216:219], v[36:39]
	v_fmac_f32_e32 v49, v62, v7
	v_mfma_f32_16x16x32_f16 v[164:167], v[180:183], v[216:219], v[168:171]
	v_or_b32_e32 v7, 0x1c880, v6
	v_exp_f32_e32 v16, v16
	v_exp_f32_e32 v2, v2
	ds_read_b128 v[36:39], v86 offset:11200
	ds_read_b128 v[168:171], v86 offset:21952
	ds_read_b128 v[180:183], v86 offset:448
	ds_read_b128 v[184:187], v86 offset:43456
	s_waitcnt lgkmcnt(9)
	v_mfma_f32_16x16x32_f16 v[156:159], v[176:179], v[228:231], v[156:159]
	v_exp_f32_e32 v3, v3
	v_add_f32_e32 v16, 1.0, v16
	v_add_f32_e32 v2, 1.0, v2
	v_mfma_f32_16x16x32_f16 v[44:47], v[176:179], v[188:191], v[44:47]
	ds_read_b128 v[176:179], v86 offset:32704
	ds_read_b128 v[212:215], v7
	v_exp_f32_e32 v7, v17
	v_rcp_f32_e32 v16, v16
	v_rcp_f32_e32 v2, v2
	v_add_f32_e32 v3, 1.0, v3
	v_add_f32_e32 v7, 1.0, v7
	s_waitcnt lgkmcnt(9)
	v_mfma_f32_16x16x32_f16 v[40:43], v[196:199], v[188:191], v[40:43]
	v_rcp_f32_e32 v7, v7
	v_rcp_f32_e32 v3, v3
	v_fmac_f32_e32 v48, v59, v16
	v_mfma_f32_16x16x32_f16 v[152:155], v[192:195], v[228:231], v[152:155]
	v_fmac_f32_e32 v49, v59, v2
	s_waitcnt lgkmcnt(6)
	v_pk_mul_f16 v200, v222, v89
	v_pk_mul_f16 v201, v223, v94
	v_mfma_f32_16x16x32_f16 v[24:27], v[192:195], v[188:191], v[24:27]
	v_pk_mul_f16 v210, v222, v84
	v_pk_mul_f16 v209, v221, v83
	v_pk_mul_f16 v211, v223, v85
	v_mfma_f32_16x16x32_f16 v[32:35], v[172:175], v[228:231], v[32:35]
	v_pk_mul_f16 v208, v220, v82
	v_fmac_f32_e32 v48, v60, v7
	v_fmac_f32_e32 v49, v60, v3
	v_mfma_f32_16x16x32_f16 v[20:23], v[224:227], v[228:231], v[20:23]
	v_mfma_f32_16x16x32_f16 v[28:31], v[224:227], v[188:191], v[28:31]
	v_mfma_f32_16x16x32_f16 v[160:163], v[196:199], v[228:231], v[160:163]
	v_pk_mul_f16 v199, v221, v88
	v_pk_mul_f16 v198, v220, v87
	v_mfma_f32_16x16x32_f16 v[164:167], v[172:175], v[188:191], v[164:167]
	v_exp_f32_e32 v3, v18
	v_or_b32_e32 v2, 0x1c8c0, v6
	ds_read_b128 v[172:175], v86 offset:512
	ds_read_b128 v[188:191], v86 offset:11264
	s_waitcnt lgkmcnt(5)
	v_mfma_f32_16x16x32_f16 v[160:163], v[180:183], v[198:201], v[160:163]
	v_add_f32_e32 v3, 1.0, v3
	v_rcp_f32_e32 v3, v3
	ds_read_b128 v[192:195], v86 offset:32768
	ds_read_b128 v[216:219], v86 offset:43520
	s_waitcnt lgkmcnt(4)
	v_pk_mul_f16 v222, v214, v79
	v_mfma_f32_16x16x32_f16 v[40:43], v[180:183], v[208:211], v[40:43]
	v_pk_mul_f16 v221, v213, v78
	v_pk_mul_f16 v223, v215, v80
	v_pk_mul_f16 v220, v212, v73
	v_mfma_f32_16x16x32_f16 v[156:159], v[36:39], v[198:201], v[156:159]
	v_pk_mul_f16 v182, v214, v76
	v_pk_mul_f16 v181, v213, v75
	v_pk_mul_f16 v183, v215, v77
	v_mfma_f32_16x16x32_f16 v[36:39], v[36:39], v[208:211], v[44:47]
	v_pk_mul_f16 v180, v212, v74
	v_fmac_f32_e32 v48, v57, v3
	v_exp_f32_e32 v3, v4
	v_mfma_f32_16x16x32_f16 v[44:47], v[168:171], v[198:201], v[152:155]
	s_nop 2
	ds_read_b128 v[152:155], v86 offset:22016
	ds_read_b128 v[212:215], v2
	v_exp_f32_e32 v2, v19
	v_exp_f32_e32 v6, v5
	v_add_f32_e32 v7, 1.0, v3
	v_rcp_f32_e32 v7, v7
	v_add_f32_e32 v2, 1.0, v2
	v_rcp_f32_e32 v2, v2
	v_add_f32_e32 v6, 1.0, v6
	v_mfma_f32_16x16x32_f16 v[16:19], v[168:171], v[208:211], v[24:27]
	v_rcp_f32_e32 v6, v6
	v_fmac_f32_e32 v48, v58, v2
	v_fmac_f32_e32 v49, v57, v7
	v_mfma_f32_16x16x32_f16 v[24:27], v[176:179], v[198:201], v[32:35]
	v_fmac_f32_e32 v49, v58, v6
	v_mfma_f32_16x16x32_f16 v[32:35], v[176:179], v[208:211], v[164:167]
	v_mfma_f32_16x16x32_f16 v[2:5], v[184:187], v[198:201], v[20:23]
	v_mfma_f32_16x16x32_f16 v[20:23], v[184:187], v[208:211], v[28:31]
	v_exp_f32_e32 v6, v8
	v_exp_f32_e32 v12, v12
	s_waitcnt lgkmcnt(5)
	v_mfma_f32_16x16x32_f16 v[28:31], v[172:175], v[220:223], v[160:163]
	v_exp_f32_e32 v13, v13
	s_nop 1
	ds_read_b128 v[160:163], v86 offset:576
	ds_read_b128 v[164:167], v86 offset:11328
	ds_read_b128 v[168:171], v86 offset:22080
	v_add_f32_e32 v12, 1.0, v12
	v_mfma_f32_16x16x32_f16 v[172:175], v[172:175], v[180:183], v[40:43]
	ds_read_b128 v[176:179], v86 offset:32832
	ds_read_b128 v[184:187], v86 offset:43584
	v_rcp_f32_e32 v12, v12
	v_exp_f32_e32 v40, v9
	v_add_f32_e32 v41, 1.0, v6
	v_rcp_f32_e32 v41, v41
	v_add_f32_e32 v13, 1.0, v13
	v_add_f32_e32 v40, 1.0, v40
	s_waitcnt lgkmcnt(9)
	v_mfma_f32_16x16x32_f16 v[156:159], v[188:191], v[220:223], v[156:159]
	v_rcp_f32_e32 v13, v13
	v_fmac_f32_e32 v48, v52, v41
	v_fmac_f32_e32 v49, v52, v12
	v_mfma_f32_16x16x32_f16 v[36:39], v[188:191], v[180:183], v[36:39]
	s_waitcnt lgkmcnt(5)
	v_pk_mul_f16 v197, v213, v149
	v_pk_mul_f16 v196, v212, v148
	v_pk_mul_f16 v199, v215, v1
	v_mfma_f32_16x16x32_f16 v[188:191], v[152:155], v[220:223], v[44:47]
	v_pk_mul_f16 v198, v214, v203
	v_pk_mul_f16 v209, v213, v147
	v_pk_mul_f16 v208, v212, v146
	v_mfma_f32_16x16x32_f16 v[6:9], v[152:155], v[180:183], v[16:19]
	v_pk_mul_f16 v211, v215, v202
	v_pk_mul_f16 v210, v214, v205
	v_fmac_f32_e32 v49, v53, v13
	v_mfma_f32_16x16x32_f16 v[16:19], v[192:195], v[220:223], v[24:27]
	s_nop 2
	v_rcp_f32_e32 v24, v40
	v_mfma_f32_16x16x32_f16 v[152:155], v[192:195], v[180:183], v[32:35]
	v_fmac_f32_e32 v48, v53, v24
	v_mfma_f32_16x16x32_f16 v[2:5], v[216:219], v[220:223], v[2:5]
	v_mfma_f32_16x16x32_f16 v[180:183], v[216:219], v[180:183], v[20:23]
	s_waitcnt lgkmcnt(4)
	v_mfma_f32_16x16x32_f16 v[40:43], v[160:163], v[196:199], v[28:31]
	v_mfma_f32_16x16x32_f16 v[44:47], v[160:163], v[208:211], v[172:175]
	s_waitcnt lgkmcnt(3)
	v_mfma_f32_16x16x32_f16 v[32:35], v[164:167], v[196:199], v[156:159]
	v_mfma_f32_16x16x32_f16 v[36:39], v[164:167], v[208:211], v[36:39]
	s_waitcnt lgkmcnt(2)
	v_mfma_f32_16x16x32_f16 v[24:27], v[168:171], v[196:199], v[188:191]
	v_mfma_f32_16x16x32_f16 v[28:31], v[168:171], v[208:211], v[6:9]
	s_waitcnt lgkmcnt(1)
	v_mfma_f32_16x16x32_f16 v[16:19], v[176:179], v[196:199], v[16:19]
	v_mfma_f32_16x16x32_f16 v[20:23], v[176:179], v[208:211], v[152:155]
	s_waitcnt lgkmcnt(0)
	v_mfma_f32_16x16x32_f16 v[6:9], v[184:187], v[196:199], v[2:5]
	v_mfma_f32_16x16x32_f16 v[2:5], v[184:187], v[208:211], v[180:183]
	v_exp_f32_e32 v12, v14
	v_exp_f32_e32 v13, v15
	v_exp_f32_e32 v10, v10
	v_exp_f32_e32 v11, v11
	v_add_f32_e32 v12, 1.0, v12
	v_rcp_f32_e32 v12, v12
	v_add_f32_e32 v13, 1.0, v13
	v_rcp_f32_e32 v13, v13
	v_add_f32_e32 v10, 1.0, v10
	v_fmac_f32_e32 v49, v51, v12
	v_mbcnt_lo_u32_b32 v12, -1, 0
	v_mbcnt_hi_u32_b32 v12, -1, v12
	v_and_b32_e32 v14, 64, v12
	v_fmac_f32_e32 v49, v56, v13
	v_xor_b32_e32 v13, 16, v12
	v_add_u32_e32 v14, 64, v14
	v_cmp_lt_i32_e64 s[0:1], v13, v14
	v_rcp_f32_e32 v10, v10
	v_add_f32_e32 v11, 1.0, v11
	v_cndmask_b32_e64 v13, v12, v13, s[0:1]
	v_lshlrev_b32_e32 v151, 2, v13
	v_rcp_f32_e32 v11, v11
	ds_bpermute_b32 v13, v151, v49
	v_fmac_f32_e32 v48, v51, v10
	v_lshlrev_b32_e32 v152, 2, v206
	v_fmac_f32_e32 v48, v56, v11
	v_xor_b32_e32 v11, 32, v12
	s_waitcnt lgkmcnt(0)
	v_add_f32_e32 v10, v49, v13
	ds_bpermute_b32 v13, v151, v48
	v_cmp_lt_i32_e64 s[0:1], v11, v14
	s_nop 1
	v_cndmask_b32_e64 v11, v12, v11, s[0:1]
	v_lshlrev_b32_e32 v153, 2, v11
	s_waitcnt lgkmcnt(0)
	v_add_f32_e32 v12, v48, v13
	ds_bpermute_b32 v11, v153, v10
	ds_bpermute_b32 v13, v153, v12
	s_and_saveexec_b64 s[0:1], vcc
	s_cbranch_execz .LBB1_27
	s_waitcnt lgkmcnt(0)
	v_add_f32_e32 v12, v12, v13
	v_add_f32_e32 v10, v10, v11
	v_add3_u32 v11, v54, v55, v152
	ds_write2_b32 v11, v10, v12 offset1:16

	.amdhsa_kernel _Z15score_ds_kernelPKfS0_S0_S0_S0_S0_PfPKDF16_
		.amdhsa_group_segment_fixed_size 121472
		.amdhsa_private_segment_fixed_size 0
		.amdhsa_kernarg_size 64
		.amdhsa_user_sgpr_count 2
		.amdhsa_user_sgpr_dispatch_ptr 0
		.amdhsa_user_sgpr_queue_ptr 0
		.amdhsa_user_sgpr_kernarg_segment_ptr 1
		.amdhsa_user_sgpr_dispatch_id 0
		.amdhsa_user_sgpr_kernarg_preload_length 0
		.amdhsa_user_sgpr_kernarg_preload_offset 0
		.amdhsa_user_sgpr_private_segment_size 0
		.amdhsa_uses_dynamic_stack 0
		.amdhsa_enable_private_segment 0
		.amdhsa_system_sgpr_workgroup_id_x 1
		.amdhsa_system_sgpr_workgroup_id_y 0
		.amdhsa_system_sgpr_workgroup_id_z 0
		.amdhsa_system_sgpr_workgroup_info 0
		.amdhsa_system_vgpr_workitem_id 0
		.amdhsa_next_free_vgpr 256
		.amdhsa_next_free_sgpr 96
		.amdhsa_accum_offset 256
		.amdhsa_reserve_vcc 1
		.amdhsa_float_round_mode_32 0
		.amdhsa_float_round_mode_16_64 0
		.amdhsa_float_denorm_mode_32 3
		.amdhsa_float_denorm_mode_16_64 3
		.amdhsa_dx10_clamp 1
		.amdhsa_ieee_mode 1
		.amdhsa_fp16_overflow 0
		.amdhsa_tg_split 0
		.amdhsa_exception_fp_ieee_invalid_op 0
		.amdhsa_exception_fp_denorm_src 0
		.amdhsa_exception_fp_ieee_div_zero 0
		.amdhsa_exception_fp_ieee_overflow 0
		.amdhsa_exception_fp_ieee_underflow 0
		.amdhsa_exception_fp_ieee_inexact 0
		.amdhsa_exception_int_div_zero 0
	.end_amdhsa_kernel

amdhsa.kernels:
  - .agpr_count:     16
    .args:
      - .actual_access:  read_only
        .address_space:  global
        .offset:         0
        .size:           8
        .value_kind:     global_buffer
      - .actual_access:  read_only
        .address_space:  global
        .offset:         8
        .size:           8
        .value_kind:     global_buffer
      - .actual_access:  read_only
        .address_space:  global
        .offset:         16
        .size:           8
        .value_kind:     global_buffer
      - .actual_access:  read_only
        .address_space:  global
        .offset:         24
        .size:           8
        .value_kind:     global_buffer
      - .actual_access:  write_only
        .address_space:  global
        .offset:         32
        .size:           8
        .value_kind:     global_buffer
      - .offset:         40
        .size:           4
        .value_kind:     by_value
      - .offset:         44
        .size:           4
        .value_kind:     by_value
      - .offset:         48
        .size:           4
        .value_kind:     by_value
      - .offset:         52
        .size:           4
        .value_kind:     by_value
      - .offset:         56
        .size:           4
        .value_kind:     by_value
      - .offset:         60
        .size:           4
        .value_kind:     by_value
      - .offset:         64
        .size:           4
        .value_kind:     by_value
    .group_segment_fixed_size: 43008
    .kernarg_segment_align: 8
    .kernarg_segment_size: 68
    .language:       OpenCL C
    .language_version:
      - 2
      - 0
    .max_flat_workgroup_size: 256
    .name:           _Z15gemm_f16_kernelPKDF16_S0_PKfS2_Pfiiiiiii
    .private_segment_fixed_size: 0
    .sgpr_count:     33
    .sgpr_spill_count: 0
    .symbol:         _Z15gemm_f16_kernelPKDF16_S0_PKfS2_Pfiiiiiii.kd
    .uniform_work_group_size: 1
    .uses_dynamic_stack: false
    .vgpr_count:     152
    .vgpr_spill_count: 0
    .wavefront_size: 64
  - .agpr_count:     0
    .args:
      - .actual_access:  read_only
        .address_space:  global
        .offset:         0
        .size:           8
        .value_kind:     global_buffer
      - .actual_access:  read_only
        .address_space:  global
        .offset:         8
        .size:           8
        .value_kind:     global_buffer
      - .actual_access:  read_only
        .address_space:  global
        .offset:         16
        .size:           8
        .value_kind:     global_buffer
      - .actual_access:  read_only
        .address_space:  global
        .offset:         24
        .size:           8
        .value_kind:     global_buffer
      - .actual_access:  read_only
        .address_space:  global
        .offset:         32
        .size:           8
        .value_kind:     global_buffer
      - .actual_access:  read_only
        .address_space:  global
        .offset:         40
        .size:           8
        .value_kind:     global_buffer
      - .actual_access:  write_only
        .address_space:  global
        .offset:         48
        .size:           8
        .value_kind:     global_buffer
      - .actual_access:  read_only
        .address_space:  global
        .offset:         56
        .size:           8
        .value_kind:     global_buffer
    .group_segment_fixed_size: 121472
    .kernarg_segment_align: 8
    .kernarg_segment_size: 64
    .language:       OpenCL C
    .language_version:
      - 2
      - 0
    .max_flat_workgroup_size: 512
    .name:           _Z15score_ds_kernelPKfS0_S0_S0_S0_S0_PfPKDF16_
    .private_segment_fixed_size: 0
    .sgpr_count:     32
    .sgpr_spill_count: 0
    .symbol:         _Z15score_ds_kernelPKfS0_S0_S0_S0_S0_PfPKDF16_.kd
    .uniform_work_group_size: 1
    .uses_dynamic_stack: false
    .vgpr_count:     256
    .vgpr_spill_count: 0
    .wavefront_size: 64
  - .agpr_count:     0
    .args:
      - .actual_access:  read_only
        .address_space:  global
        .offset:         0
        .size:           8
        .value_kind:     global_buffer
      - .actual_access:  read_only
        .address_space:  global
        .offset:         8
        .size:           8
        .value_kind:     global_buffer
      - .actual_access:  read_only
        .address_space:  global
        .offset:         16
        .size:           8
        .value_kind:     global_buffer
      - .actual_access:  read_only
        .address_space:  global
        .offset:         24
        .size:           8
        .value_kind:     global_buffer
      - .actual_access:  read_only
        .address_space:  global
        .offset:         32
        .size:           8
        .value_kind:     global_buffer
      - .actual_access:  read_only
        .address_space:  global
        .offset:         40
        .size:           8
        .value_kind:     global_buffer
      - .actual_access:  read_only
        .address_space:  global
        .offset:         48
        .size:           8
        .value_kind:     global_buffer
      - .actual_access:  read_only
        .address_space:  global
        .offset:         56
        .size:           8
        .value_kind:     global_buffer
      - .actual_access:  read_only
        .address_space:  global
        .offset:         64
        .size:           8
        .value_kind:     global_buffer
      - .actual_access:  read_only
        .address_space:  global
        .offset:         72
        .size:           8
        .value_kind:     global_buffer
      - .actual_access:  write_only
        .address_space:  global
        .offset:         80
        .size:           8
        .value_kind:     global_buffer
    .group_segment_fixed_size: 94336
    .kernarg_segment_align: 8
    .kernarg_segment_size: 88
    .language:       OpenCL C
    .language_version:
      - 2
      - 0
    .max_flat_workgroup_size: 1024
    .name:           _Z13attend_kernelPKfS0_S0_S0_S0_S0_S0_S0_S0_S0_PDF16_
    .private_segment_fixed_size: 0
    .sgpr_count:     40
    .sgpr_spill_count: 0
    .symbol:         _Z13attend_kernelPKfS0_S0_S0_S0_S0_S0_S0_S0_S0_PDF16_.kd
    .uniform_work_group_size: 1
    .uses_dynamic_stack: false
    .vgpr_count:     128
    .vgpr_spill_count: 0
    .wavefront_size: 64
  - .agpr_count:     0
    .args:
      - .actual_access:  read_only
        .address_space:  global
        .offset:         0
        .size:           8
        .value_kind:     global_buffer
      - .actual_access:  read_only
        .address_space:  global
        .offset:         8
        .size:           8
        .value_kind:     global_buffer
      - .actual_access:  read_only
        .address_space:  global
        .offset:         16
        .size:           8
        .value_kind:     global_buffer
      - .actual_access:  read_only
        .address_space:  global
        .offset:         24
        .size:           8
        .value_kind:     global_buffer
      - .actual_access:  write_only
        .address_space:  global
        .offset:         32
        .size:           8
        .value_kind:     global_buffer
    .group_segment_fixed_size: 9088
    .kernarg_segment_align: 8
    .kernarg_segment_size: 40
    .language:       OpenCL C
    .language_version:
      - 2
      - 0
    .max_flat_workgroup_size: 512
    .name:           _Z16postfinal_kernelPKfS0_S0_S0_Pf
    .private_segment_fixed_size: 0
    .sgpr_count:     30
    .sgpr_spill_count: 0
    .symbol:         _Z16postfinal_kernelPKfS0_S0_S0_Pf.kd
    .uniform_work_group_size: 1
    .uses_dynamic_stack: false
    .vgpr_count:     124
    .vgpr_spill_count: 0
    .wavefront_size: 64
  - .agpr_count:     16
    .args:
      - .offset:         0
        .size:           1136
        .value_kind:     by_value
    .group_segment_fixed_size: 34816
    .kernarg_segment_align: 8
    .kernarg_segment_size: 1136
    .language:       OpenCL C
    .language_version:
      - 2
      - 0
    .max_flat_workgroup_size: 256
    .name:           _Z14gemm_nt_kernelILi2EEv8GemmArgs
    .private_segment_fixed_size: 0
    .sgpr_count:     68
    .sgpr_spill_count: 0
    .symbol:         _Z14gemm_nt_kernelILi2EEv8GemmArgs.kd
    .uniform_work_group_size: 1
    .uses_dynamic_stack: false
    .vgpr_count:     140
    .vgpr_spill_count: 0
    .wavefront_size: 64
  - .agpr_count:     0
    .args:
      - .actual_access:  read_only
        .address_space:  global
        .offset:         0
        .size:           8
        .value_kind:     global_buffer
      - .offset:         8
        .size:           8
        .value_kind:     by_value
      - .actual_access:  read_only
        .address_space:  global
        .offset:         16
        .size:           8
        .value_kind:     global_buffer
      - .actual_access:  read_only
        .address_space:  global
        .offset:         24
        .size:           8
        .value_kind:     global_buffer
      - .actual_access:  read_only
        .address_space:  global
        .offset:         32
        .size:           8
        .value_kind:     global_buffer
      - .actual_access:  read_only
        .address_space:  global
        .offset:         40
        .size:           8
        .value_kind:     global_buffer
      - .actual_access:  write_only
        .address_space:  global
        .offset:         48
        .size:           8
        .value_kind:     global_buffer
      - .actual_access:  write_only
        .address_space:  global
        .offset:         56
        .size:           8
        .value_kind:     global_buffer
      - .offset:         64
        .size:           4
        .value_kind:     by_value
      - .offset:         72
        .size:           376
        .value_kind:     by_value
    .group_segment_fixed_size: 63488
    .kernarg_segment_align: 8
    .kernarg_segment_size: 448
    .language:       OpenCL C
    .language_version:
      - 2
      - 0
    .max_flat_workgroup_size: 512
    .name:           _Z15gru_mfma_kernelILi1EEvPKfmS1_S1_S1_S1_PfS2_i7PreArgs
    .private_segment_fixed_size: 0
    .sgpr_count:     36
    .sgpr_spill_count: 0
    .symbol:         _Z15gru_mfma_kernelILi1EEvPKfmS1_S1_S1_S1_PfS2_i7PreArgs.kd
    .uniform_work_group_size: 1
    .uses_dynamic_stack: false
    .vgpr_count:     232
    .vgpr_spill_count: 0
    .wavefront_size: 64
  - .agpr_count:     0
    .args:
      - .actual_access:  read_only
        .address_space:  global
        .offset:         0
        .size:           8
        .value_kind:     global_buffer
      - .offset:         8
        .size:           8
        .value_kind:     by_value
      - .actual_access:  read_only
        .address_space:  global
        .offset:         16
        .size:           8
        .value_kind:     global_buffer
      - .actual_access:  read_only
        .address_space:  global
        .offset:         24
        .size:           8
        .value_kind:     global_buffer
      - .actual_access:  read_only
        .address_space:  global
        .offset:         32
        .size:           8
        .value_kind:     global_buffer
      - .actual_access:  read_only
        .address_space:  global
        .offset:         40
        .size:           8
        .value_kind:     global_buffer
      - .actual_access:  write_only
        .address_space:  global
        .offset:         48
        .size:           8
        .value_kind:     global_buffer
      - .actual_access:  write_only
        .address_space:  global
        .offset:         56
        .size:           8
        .value_kind:     global_buffer
      - .offset:         64
        .size:           4
        .value_kind:     by_value
      - .offset:         72
        .size:           376
        .value_kind:     by_value
    .group_segment_fixed_size: 64480
    .kernarg_segment_align: 8
    .kernarg_segment_size: 448
    .language:       OpenCL C
    .language_version:
      - 2
      - 0
    .max_flat_workgroup_size: 512
    .name:           _Z15gru_mfma_kernelILi2EEvPKfmS1_S1_S1_S1_PfS2_i7PreArgs
    .private_segment_fixed_size: 0
    .sgpr_count:     50
    .sgpr_spill_count: 0
    .symbol:         _Z15gru_mfma_kernelILi2EEvPKfmS1_S1_S1_S1_PfS2_i7PreArgs.kd
    .uniform_work_group_size: 1
    .uses_dynamic_stack: false
    .vgpr_count:     232
    .vgpr_spill_count: 0
    .wavefront_size: 64
